# same as previous best but the in-projection / out-projection start-up staggers set to zero (workgroups sharing L2 tiles stay in phase)
# speedup vs baseline: 1.0001x; 1.0001x over previous
.LBB0_219:
	s_cmp_lt_i32 s92, 4
	s_cselect_b64 s[0:1], -1, 0
	s_cmp_gt_i32 s93, 3
	s_cselect_b64 s[2:3], -1, 0
	s_and_b64 s[0:1], s[0:1], s[2:3]
	v_writelane_b32 v254, s90, 8
	v_cndmask_b32_e64 v0, 0, 1, s[0:1]
	v_cmp_ne_u32_e64 s[2:3], 1, v0
	v_writelane_b32 v254, s91, 9
	s_andn2_b64 vcc, exec, s[0:1]
	v_writelane_b32 v254, s52, 10
	v_mbcnt_lo_u32_b32 v0, -1, 0
	v_mbcnt_hi_u32_b32 v0, -1, v0
	s_cbranch_vccnz .LBB0_1091
	s_load_dword s5, s[90:91], 0x100
	v_writelane_b32 v254, s2, 11
	s_lshl_b32 s0, s94, 3
	s_movk_i32 s34, 0xb8
	v_writelane_b32 v254, s3, 12
	s_add_i32 s3, s97, s0
	s_lshl_b32 s0, s97, 14
	s_waitcnt lgkmcnt(0)
	s_lshl_b32 s41, s5, 3
	s_add_i32 s0, s0, 0
	v_writelane_b32 v254, s92, 13
	s_cmp_lt_i32 s3, 0x18000
	s_cselect_b64 s[6:7], -1, 0
	v_writelane_b32 v254, s93, 14
	s_cmp_lt_u32 s3, 0x10000
	v_writelane_b32 v254, s6, 15
	s_cselect_b32 s1, s34, 0xc8
	s_cmpk_gt_u32 s3, 0x7fff
	v_writelane_b32 v254, s7, 16
	s_cselect_b32 s1, s1, 0xa8
	v_writelane_b32 v254, s1, 17
	s_lshl_b32 s1, s3, 5
	s_lshl_b32 s2, s3, 1
	v_writelane_b32 v254, s3, 19
	s_lshl_b32 s3, s3, 12
	s_ashr_i32 s4, s94, 4
	s_and_b32 s1, s1, 0x7e0
	s_and_b32 s2, s2, 0x780
	s_and_b32 s3, s3, 0x7c00000
	s_and_b32 s4, s4, -4
	s_cmpk_eq_i32 s5, 0x100
	s_cselect_b32 s35, s4, 0
	s_add_u32 s6, s26, 0x900000
	v_ashrrev_i32_e32 v1, 1, v0
	s_addc_u32 s7, s27, 0
	v_and_b32_e32 v208, -4, v1
	s_add_u32 s22, s26, 0x63800000
	v_add_u32_e32 v2, s2, v208
	s_addc_u32 s23, s27, 0
	v_ashrrev_i32_e32 v3, 31, v2
	v_lshlrev_b32_e32 v1, 2, v0
	s_add_u32 s28, s26, 0x67800000
	v_lshlrev_b64 v[176:177], 13, v[2:3]
	v_and_b32_e32 v2, 28, v1
	v_and_b32_e32 v1, 7, v0
	s_addc_u32 s29, s27, 0
	v_ashrrev_i32_e32 v209, 3, v0
	v_lshlrev_b32_e32 v180, 4, v1
	s_add_u32 s30, s26, 0x6c000000
	v_lshl_add_u32 v0, v209, 2, s0
	v_mul_u32_u24_e32 v3, 0x210, v1
	v_add_u32_e32 v1, s0, v180
	s_movk_i32 s0, 0x84
	v_writelane_b32 v254, s6, 21
	s_addc_u32 s31, s27, 0
	s_ashr_i32 s78, s94, 31
	v_mul_lo_u32 v4, v209, s0
	v_writelane_b32 v254, s7, 22
	s_add_u32 s0, s26, 0x34000000
	v_writelane_b32 v254, s0, 23
	s_addc_u32 s0, s27, 0
	v_writelane_b32 v254, s0, 25
	s_add_u32 s0, s26, 0x1000000
	v_writelane_b32 v254, s0, 27
	s_addc_u32 s0, s27, 0
	v_writelane_b32 v254, s0, 29
	s_bfe_u32 s0, s94, 0x30003
	s_mul_i32 s44, s0, 0
	s_lshl_b32 s0, s94, 15
	s_lshl_b32 s2, s97, 12
	s_add_i32 s0, s0, s2
	v_writelane_b32 v254, s0, 31
	s_lshl_b32 s0, s94, 8
	s_lshl_b32 s2, s97, 5
	s_add_i32 s0, s0, s2
	v_writelane_b32 v254, s0, 33
	s_lshl_b32 s0, s94, 4
	s_lshl_b32 s2, s97, 1
	v_writelane_b32 v254, s97, 35
	s_add_i32 s0, s0, s2
	v_writelane_b32 v254, s0, 36
	s_lshl_b32 s0, s3, 2
	v_writelane_b32 v254, s0, 38
	s_lshl_b32 s0, s1, 2
	v_writelane_b32 v254, s0, 39
	s_mov_b32 s17, 0
	s_mov_b32 s45, s17
	v_writelane_b32 v254, s1, 40
	v_writelane_b32 v254, s35, 41
	v_writelane_b32 v254, s44, 43
	s_lshl_b32 s37, s5, 16
	s_lshl_b32 s48, s5, 9
	v_writelane_b32 v254, s45, 44
	v_writelane_b32 v254, s37, 45
	s_lshl_b32 s49, s5, 5
	v_writelane_b32 v254, s48, 47
	s_lshl_b32 s50, s5, 8
	v_writelane_b32 v254, s49, 49
	v_mov_b32_e32 v179, 0
	s_lshl_b32 s51, s5, 15
	v_writelane_b32 v254, s50, 51
	s_movk_i32 s76, 0x100
	v_mov_b32_e32 v181, v179
	v_add_u32_e32 v210, 8, v209
	v_add_u32_e32 v211, 16, v209
	v_add_u32_e32 v212, 24, v209
	s_mov_b32 s92, s94
	s_lshl_b32 s89, s5, 4
	s_mov_b64 s[54:55], -1
	s_mov_b64 s[6:7], 0
	s_movk_i32 s93, 0x2000
	s_movk_i32 s94, 0x4000
	s_movk_i32 s95, 0x6000
	s_mov_b32 s96, 0x40000
	s_mov_b32 s97, 0x42000
	s_mov_b32 s4, 0x44000
	s_mov_b32 s5, 0x46000
	s_mov_b32 s75, 0x80000
	s_mov_b32 s38, 0x82000
	s_mov_b32 s83, 0x84000
	s_mov_b32 s85, 0x86000
	s_mov_b32 s87, 0xc0000
	s_mov_b32 s53, 0xc2000
	s_mov_b32 s56, 0xc4000
	s_mov_b32 s57, 0xc6000
	s_brev_b32 s58, 36
	s_movk_i32 s39, 0x600
	s_mov_b32 s40, 0x3d800000
	s_movk_i32 s77, 0x7ff
	s_mov_b32 s84, 0x9000
	v_lshlrev_b32_e32 v178, 2, v2
	v_add_u32_e32 v213, v0, v3
	v_add_u32_e32 v214, v1, v4
	v_mov_b64_e32 v[182:183], 0xcbf
	v_mov_b32_e32 v215, 1
	v_mov_b32_e32 v216, 0xbbb906ce
	v_mov_b32_e32 v217, 0xbc3963d9
	v_mov_b32_e32 v218, 0x7e0
	v_mov_b32_e32 v219, 0xa0
	v_writelane_b32 v254, s51, 53
	s_branch .LBB0_223

.LBB0_1647:
	s_memrealtime s[6:7]
	s_memrealtime s[12:13]
	s_waitcnt lgkmcnt(0)
	s_bfe_u32 s8, s94, 0x30003
	s_mov_b32 s9, 0
	s_mulk_i32 s8, 0x0
	v_mov_b64_e32 v[0:1], s[8:9]
	s_sub_u32 s12, s12, s6
	s_subb_u32 s13, s13, s7
	v_cmp_ge_u64_e32 vcc, s[12:13], v[0:1]
	s_cbranch_vccnz .LBB0_1650
	v_mov_b64_e32 v[0:1], s[8:9]
